# speedup vs baseline: 1.0064x; 1.0064x over previous
_Z7gemm_x3ILi2ELi2ELi2ELi0EEvPKcS1_iiPKfiS3_PKiPciPy:
	s_load_dwordx8 s[4:11], s[0:1], 0x0
	s_ashr_i32 s17, s2, 3
	s_abs_i32 s18, s17
	v_lshlrev_b32_e32 v170, 4, v0
	s_load_dword s16, s[0:1], 0x20
	s_load_dwordx4 s[12:15], s[0:1], 0x28
	s_waitcnt lgkmcnt(0)
	s_load_dword s30, s[0:1], 0x40
	s_abs_i32 s3, s9
	v_cvt_f32_u32_e32 v2, s3
	s_sub_i32 s20, 0, s3
	s_xor_b32 s19, s17, s9
	s_ashr_i32 s19, s19, 31
	v_rcp_iflag_f32_e32 v2, v2
	v_bfe_u32 v19, v0, 6, 1
	v_and_b32_e32 v164, 31, v0
	v_mov_b32_e32 v155, 0
	v_mul_f32_e32 v2, 0x4f7ffffe, v2
	v_cvt_u32_f32_e32 v2, v2
	v_lshlrev_b32_e32 v165, 6, v19
	v_mov_b32_e32 v3, v155
	v_bfe_u32 v1, v0, 7, 1
	v_readfirstlane_b32 s21, v2
	s_mul_i32 s20, s20, s21
	s_mul_hi_u32 s20, s21, s20
	s_add_i32 s21, s21, s20
	s_mul_hi_u32 s20, s18, s21
	s_mul_i32 s21, s20, s3
	s_sub_i32 s18, s18, s21
	s_add_i32 s22, s20, 1
	s_sub_i32 s21, s18, s3
	s_cmp_ge_u32 s18, s3
	s_cselect_b32 s20, s22, s20
	s_cselect_b32 s18, s21, s18
	s_add_i32 s21, s20, 1
	s_cmp_ge_u32 s18, s3
	s_cselect_b32 s3, s21, s20
	s_xor_b32 s3, s3, s19
	s_sub_i32 s20, s3, s19
	s_mul_i32 s3, s20, s9
	s_sub_i32 s3, s17, s3
	s_lshl_b32 s2, s2, 7
	s_lshl_b32 s3, s3, 10
	s_and_b32 s2, s2, 0x380
	s_or_b32 s17, s3, s2
	s_ashr_i32 s9, s17, 7
	s_ashr_i32 s2, s8, 6
	s_ashr_i32 s18, s9, 31
	s_ashr_i32 s3, s2, 31
	s_lshl_b32 s21, s2, 14
	s_mul_i32 s18, s21, s18
	s_mul_hi_u32 s19, s21, s9
	s_lshr_b64 s[2:3], s[2:3], 18
	s_add_i32 s18, s19, s18
	s_mul_i32 s3, s2, s9
	s_add_i32 s3, s18, s3
	s_mul_i32 s9, s21, s9
	s_add_u32 s18, s6, s9
	s_addc_u32 s19, s7, s3
	s_movk_i32 s3, 0x70
	v_bitop3_b32 v154, v0, s3, v170 bitop3:0x48
	s_ashr_i32 s3, s20, 31
	s_mul_i32 s3, s21, s3
	s_mul_hi_u32 s6, s21, s20
	s_add_i32 s3, s6, s3
	s_mul_i32 s2, s2, s20
	s_add_i32 s6, s3, s2
	s_mul_i32 s7, s21, s20
	s_add_u32 s2, s4, s7
	s_addc_u32 s3, s5, s6
	v_and_b32_e32 v2, 0x1f80, v170
	v_or3_b32 v6, v165, s17, v164
	v_lshl_add_u64 v[4:5], s[2:3], 0, v[2:3]
	v_ashrrev_i32_e32 v7, 31, v6
	v_lshl_add_u64 v[146:147], v[4:5], 0, v[154:155]
	s_movk_i32 s9, 0x3f80
	v_mov_b32_e32 v4, 0x2000
	v_lshrrev_b32_e32 v168, 8, v0
	v_bfe_u32 v18, v0, 5, 1
	v_lshl_add_u64 v[6:7], v[6:7], 2, s[14:15]
	v_lshlrev_b32_e32 v166, 6, v1
	v_bitop3_b32 v4, v170, s9, v4 bitop3:0xc8
	global_load_dword v20, v[6:7], off
	global_load_dword v21, v[6:7], off offset:128
	s_lshl_b32 s9, s20, 7
	v_lshl_or_b32 v6, v168, 5, v166
	v_lshlrev_b32_e32 v167, 2, v18
	v_or3_b32 v14, v6, v167, s9
	v_cmp_gt_i32_e32 vcc, s16, v14
	v_or_b32_e32 v10, 8, v14
	v_mov_b32_e32 v5, v155
	v_cndmask_b32_e32 v6, 0, v14, vcc
	v_cmp_gt_i32_e32 vcc, s16, v10
	v_ashrrev_i32_e32 v7, 31, v6
	v_lshlrev_b64 v[6:7], 2, v[6:7]
	v_cndmask_b32_e32 v10, 0, v10, vcc
	v_ashrrev_i32_e32 v11, 31, v10
	v_lshl_add_u64 v[8:9], s[10:11], 0, v[6:7]
	v_lshlrev_b64 v[10:11], 2, v[10:11]
	v_lshl_add_u64 v[12:13], s[10:11], 0, v[10:11]
	global_load_dwordx4 v[78:81], v[8:9], off
	global_load_dwordx4 v[74:77], v[12:13], off
	v_or_b32_e32 v8, 16, v14
	v_cmp_gt_i32_e32 vcc, s16, v8
	v_or_b32_e32 v14, 24, v14
	v_lshl_add_u64 v[156:157], s[2:3], 0, v[4:5]
	s_movk_i32 s2, 0x7f80
	v_mov_b32_e32 v4, 0x6000
	v_cndmask_b32_e32 v8, 0, v8, vcc
	v_cmp_gt_i32_e32 vcc, s16, v14
	v_bitop3_b32 v4, v170, s2, v4 bitop3:0xc8
	v_ashrrev_i32_e32 v9, 31, v8
	v_cndmask_b32_e32 v14, 0, v14, vcc
	v_lshl_add_u64 v[160:161], s[18:19], 0, v[4:5]
	s_movk_i32 s2, 0xc000
	v_lshlrev_b64 v[8:9], 2, v[8:9]
	v_ashrrev_i32_e32 v15, 31, v14
	v_lshl_add_u64 v[4:5], v[160:161], 0, v[154:155]
	s_mov_b32 s3, -1
	v_lshl_add_u64 v[12:13], s[10:11], 0, v[8:9]
	v_lshlrev_b64 v[14:15], 2, v[14:15]
	v_add_u32_e32 v178, 0, v170
	v_lshl_add_u64 v[152:153], v[4:5], 0, s[2:3]
	v_lshl_add_u64 v[16:17], s[10:11], 0, v[14:15]
	global_load_dwordx4 v[70:73], v[12:13], off
	global_load_dwordx4 v[66:69], v[16:17], off
	v_readfirstlane_b32 s2, v178
	v_add_u32_e32 v12, 0x2000, v178
	s_mov_b32 m0, s2
	v_readfirstlane_b32 s2, v12
	v_add_u32_e32 v12, 0x4000, v178
	v_lshl_add_u64 v[150:151], v[156:157], 0, v[154:155]
	v_lshl_add_u64 v[158:159], s[18:19], 0, v[2:3]
	global_load_lds_dwordx4 v[146:147], off
	s_mov_b32 m0, s2
	v_readfirstlane_b32 s2, v12
	v_add_u32_e32 v12, 0x6000, v178
	v_lshl_add_u64 v[148:149], v[158:159], 0, v[154:155]
	global_load_lds_dwordx4 v[150:151], off
	s_mov_b32 m0, s2
	v_readfirstlane_b32 s2, v12
	v_add_u32_e32 v16, 0x8000, v178
	global_load_lds_dwordx4 v[148:149], off
	s_mov_b32 m0, s2
	s_mov_b64 s[10:11], 0x4000
	v_readfirstlane_b32 s2, v16
	v_add_u32_e32 v16, 0xa000, v178
	global_load_lds_dwordx4 v[152:153], off
	v_lshl_add_u64 v[12:13], v[146:147], 0, s[10:11]
	s_mov_b32 m0, s2
	v_readfirstlane_b32 s2, v16
	v_add_u32_e32 v16, 0xc000, v178
	global_load_lds_dwordx4 v[12:13], off
	v_lshl_add_u64 v[12:13], v[150:151], 0, s[10:11]
	s_mov_b32 m0, s2
	v_readfirstlane_b32 s2, v16
	global_load_lds_dwordx4 v[12:13], off
	v_lshl_add_u64 v[12:13], v[148:149], 0, s[10:11]
	s_mov_b32 m0, s2
	v_lshlrev_b32_e32 v169, 13, v19
	global_load_lds_dwordx4 v[12:13], off
	v_add_u32_e32 v12, 0xe000, v178
	s_nop 0
	v_readfirstlane_b32 s2, v12
	s_mov_b32 m0, s2
	s_add_i32 s2, 0, 0x10000
	v_add_u32_e32 v16, s2, v170
	s_mov_b64 s[2:3], 0x8000
	v_readfirstlane_b32 s14, v16
	v_add_u32_e32 v17, 0x2000, v16
	global_load_lds_dwordx4 v[4:5], off
	v_lshl_add_u64 v[12:13], v[146:147], 0, s[2:3]
	s_mov_b32 m0, s14
	v_readfirstlane_b32 s14, v17
	v_add_u32_e32 v17, 0x4000, v16
	global_load_lds_dwordx4 v[12:13], off
	v_lshl_add_u64 v[12:13], v[150:151], 0, s[2:3]
	s_mov_b32 m0, s14
	v_readfirstlane_b32 s14, v17
	global_load_lds_dwordx4 v[12:13], off
	v_lshl_add_u64 v[12:13], v[148:149], 0, s[2:3]
	s_mov_b32 m0, s14
	v_lshl_add_u64 v[4:5], v[4:5], 0, s[10:11]
	global_load_lds_dwordx4 v[12:13], off
	v_add_u32_e32 v12, 0x6000, v16
	s_mov_b32 s14, 0
	v_readfirstlane_b32 s10, v12
	s_mov_b32 m0, s10
	s_load_dwordx2 s[10:11], s[0:1], 0x38
	global_load_lds_dwordx4 v[4:5], off
	s_mov_b64 s[24:25], 0xc000
	v_add_u32_e32 v180, 0x18000, v170
	v_add_u32_e32 v181, 0x1a000, v170
	v_add_u32_e32 v182, 0x1c000, v170
	v_add_u32_e32 v183, 0x1e000, v170
	v_lshl_add_u64 v[12:13], v[146:147], 0, s[24:25]
	v_lshl_add_u64 v[16:17], v[150:151], 0, s[24:25]
	v_readfirstlane_b32 s26, v180
	v_readfirstlane_b32 s27, v181
	v_readfirstlane_b32 s28, v182
	v_readfirstlane_b32 s29, v183
	s_mov_b32 m0, s26
	v_lshl_add_u64 v[184:185], v[148:149], 0, s[24:25]
	global_load_lds_dwordx4 v[12:13], off
	s_mov_b32 m0, s27
	v_lshl_add_u64 v[186:187], v[152:153], 0, s[24:25]
	global_load_lds_dwordx4 v[16:17], off
	s_mov_b32 m0, s28
	s_nop 0
	global_load_lds_dwordx4 v[184:185], off
	s_mov_b32 m0, s29
	s_nop 0
	global_load_lds_dwordx4 v[186:187], off
	v_lshlrev_b32_e32 v4, 2, v168
	v_bfe_u32 v5, v0, 1, 3
	v_bitop3_b32 v4, v4, v5, v18 bitop3:0x36
	v_lshlrev_b32_e32 v22, 4, v4
	v_lshlrev_b32_e32 v4, 7, v164
	v_lshl_or_b32 v5, v1, 13, v4
	v_or_b32_e32 v24, v169, v4
	v_add_u32_e32 v171, v5, v22
	v_or_b32_e32 v5, 0x4000, v22
	v_or_b32_e32 v26, 0x1000, v24
	v_add_u32_e32 v23, 0x1000, v171
	v_add_u32_e32 v25, v5, v24
	v_add_u32_e32 v27, v5, v26
	s_waitcnt vmcnt(12)
	s_barrier
	v_add_u32_e32 v12, 0x800, v20
	s_movk_i32 s15, 0xfa0
	v_mov_b64_e32 v[4:5], s[12:13]
	v_mad_i64_i32 v[12:13], s[12:13], v12, s15, v[4:5]
	v_lshl_add_u64 v[16:17], v[12:13], 0, v[6:7]
	v_lshl_add_u64 v[18:19], v[12:13], 0, v[10:11]
	global_load_dwordx4 v[110:113], v[16:17], off
	global_load_dwordx4 v[106:109], v[18:19], off
	v_lshl_add_u64 v[16:17], v[12:13], 0, v[8:9]
	v_lshl_add_u64 v[12:13], v[12:13], 0, v[14:15]
	global_load_dwordx4 v[102:105], v[16:17], off
	global_load_dwordx4 v[98:101], v[12:13], off
	v_add_u32_e32 v12, 0x800, v21
	v_mad_i64_i32 v[4:5], s[12:13], v12, s15, v[4:5]
	v_lshl_add_u64 v[6:7], v[4:5], 0, v[6:7]
	v_lshl_add_u64 v[10:11], v[4:5], 0, v[10:11]
	global_load_dwordx4 v[94:97], v[6:7], off
	global_load_dwordx4 v[90:93], v[10:11], off
	v_lshl_add_u64 v[6:7], v[4:5], 0, v[8:9]
	v_lshl_add_u64 v[4:5], v[4:5], 0, v[14:15]
	global_load_dwordx4 v[86:89], v[6:7], off
	global_load_dwordx4 v[82:85], v[4:5], off
	v_add_u32_e32 v4, 0, v171
	v_add_u32_e32 v172, v22, v24
	ds_read_b128 v[130:133], v4
	ds_read_b128 v[126:129], v4 offset:4096
	v_add_u32_e32 v4, 0, v172
	v_add_u32_e32 v174, v22, v26
	v_xor_b32_e32 v177, 32, v171
	v_add_u32_e32 v5, 0, v174
	ds_read_b128 v[142:145], v4 offset:16384
	ds_read_b128 v[138:141], v5 offset:16384
	v_add_u32_e32 v4, 0, v177
	v_xor_b32_e32 v175, 32, v23
	v_xor_b32_e32 v173, 32, v25
	v_xor_b32_e32 v176, 32, v27
	v_add_u32_e32 v5, 0, v175
	v_add_u32_e32 v6, 0, v173
	v_add_u32_e32 v7, 0, v176
	ds_read_b128 v[134:137], v4
	ds_read_b128 v[114:117], v5
	ds_read_b128 v[122:125], v6
	ds_read_b128 v[118:121], v7
	s_cmpk_lt_i32 s8, 0x140
	s_cbranch_scc1 .LBB5_3
	s_ashr_i32 s12, s8, 31
	s_lshr_b32 s12, s12, 26
	s_add_i32 s8, s8, s12
	s_ashr_i32 s8, s8, 6
	s_add_i32 s8, s8, -4
	s_add_u32 s4, s4, s7
	s_addc_u32 s5, s5, s6
	v_lshl_add_u64 v[162:163], s[4:5], 0, v[2:3]
	s_mov_b64 s[24:25], 0x4000
	v_lshl_add_u64 v[162:163], v[162:163], 0, s[24:25]
	v_lshl_add_u64 v[156:157], v[156:157], 0, s[24:25]
	v_lshl_add_u64 v[158:159], v[158:159], 0, s[24:25]
	v_lshl_add_u64 v[160:161], v[160:161], 0, s[24:25]
	v_mov_b32_e32 v2, 0
	s_mov_b32 s12, 0x18000
	s_mov_b64 s[4:5], 0xc000
	s_mov_b64 s[6:7], 0x10000
	v_mov_b32_e32 v3, v2
	v_mov_b32_e32 v4, v2
	v_mov_b32_e32 v5, v2
	v_mov_b32_e32 v6, v2
	v_mov_b32_e32 v7, v2
	v_mov_b32_e32 v8, v2
	v_mov_b32_e32 v9, v2
	v_mov_b32_e32 v10, v2
	v_mov_b32_e32 v11, v2
	v_mov_b32_e32 v12, v2
	v_mov_b32_e32 v13, v2
	v_mov_b32_e32 v14, v2
	v_mov_b32_e32 v15, v2
	v_mov_b32_e32 v16, v2
	v_mov_b32_e32 v17, v2
	v_mov_b32_e32 v18, v2
	v_mov_b32_e32 v19, v2
	v_mov_b32_e32 v20, v2
	v_mov_b32_e32 v21, v2
	v_mov_b32_e32 v22, v2
	v_mov_b32_e32 v23, v2
	v_mov_b32_e32 v24, v2
	v_mov_b32_e32 v25, v2
	v_mov_b32_e32 v26, v2
	v_mov_b32_e32 v27, v2
	v_mov_b32_e32 v28, v2
	v_mov_b32_e32 v29, v2
	v_mov_b32_e32 v30, v2
	v_mov_b32_e32 v31, v2
	v_mov_b32_e32 v32, v2
	v_mov_b32_e32 v33, v2
	v_mov_b32_e32 v34, v2
	v_mov_b32_e32 v35, v2
	v_mov_b32_e32 v36, v2
	v_mov_b32_e32 v37, v2
	v_mov_b32_e32 v38, v2
	v_mov_b32_e32 v39, v2
	v_mov_b32_e32 v40, v2
	v_mov_b32_e32 v41, v2
	v_mov_b32_e32 v42, v2
	v_mov_b32_e32 v43, v2
	v_mov_b32_e32 v44, v2
	v_mov_b32_e32 v45, v2
	v_mov_b32_e32 v46, v2
	v_mov_b32_e32 v47, v2
	v_mov_b32_e32 v48, v2
	v_mov_b32_e32 v49, v2
	v_mov_b32_e32 v50, v2
	v_mov_b32_e32 v51, v2
	v_mov_b32_e32 v52, v2
	v_mov_b32_e32 v53, v2
	v_mov_b32_e32 v54, v2
	v_mov_b32_e32 v55, v2
	v_mov_b32_e32 v56, v2
	v_mov_b32_e32 v57, v2
	v_mov_b32_e32 v58, v2
	v_mov_b32_e32 v59, v2
	v_mov_b32_e32 v60, v2
	v_mov_b32_e32 v61, v2
	v_mov_b32_e32 v62, v2
	v_mov_b32_e32 v63, v2
	v_mov_b32_e32 v64, v2
	v_mov_b32_e32 v65, v2

.LBB5_8:
	s_or_b64 exec, exec, s[6:7]
	s_mov_b32 s14, s30
	v_lshlrev_b32_e32 v0, 13, v154
	v_lshlrev_b32_e32 v1, 2, v155
	v_add3_u32 v130, 0, v0, v1
	v_or_b32_e32 v0, v166, v167
	v_or_b32_e32 v131, s9, v0
	s_waitcnt lgkmcnt(0)
	s_barrier
	s_and_saveexec_b64 s[8:9], s[2:3]
	s_cbranch_execnz .LBB5_11
	s_or_b64 exec, exec, s[8:9]
	s_and_saveexec_b64 s[0:1], vcc
	s_cbranch_execnz .LBB5_28

_Z7gemm_x3ILi2ELi2ELi1ELi1EEvPKcS1_iiPKfiS3_PKiPciPy:
	s_load_dwordx8 s[4:11], s[0:1], 0x0
	s_ashr_i32 s17, s2, 3
	s_abs_i32 s15, s17
	v_lshlrev_b32_e32 v93, 4, v0
	v_mov_b32_e32 v81, 0
	s_waitcnt lgkmcnt(0)
	s_abs_i32 s3, s9
	v_cvt_f32_u32_e32 v1, s3
	s_xor_b32 s16, s17, s9
	s_ashr_i32 s18, s16, 31
	s_sub_i32 s16, 0, s3
	v_rcp_iflag_f32_e32 v2, v1
	v_mov_b64_e32 v[4:5], s[4:5]
	s_load_dword s14, s[0:1], 0x20
	s_load_dwordx2 s[12:13], s[0:1], 0x38
	v_bfe_u32 v1, v0, 7, 1
	v_mul_f32_e32 v2, 0x4f7ffffe, v2
	v_cvt_u32_f32_e32 v2, v2
	v_lshrrev_b32_e32 v90, 8, v0
	v_lshlrev_b32_e32 v88, 6, v1
	v_add_u32_e32 v99, 0, v93
	v_readfirstlane_b32 s19, v2
	s_mul_i32 s16, s16, s19
	s_mul_hi_u32 s16, s19, s16
	s_add_i32 s19, s19, s16
	s_mul_hi_u32 s16, s15, s19
	s_mul_i32 s19, s16, s3
	s_sub_i32 s15, s15, s19
	s_add_i32 s20, s16, 1
	s_sub_i32 s19, s15, s3
	s_cmp_ge_u32 s15, s3
	s_cselect_b32 s16, s20, s16
	s_cselect_b32 s15, s19, s15
	s_add_i32 s19, s16, 1
	s_cmp_ge_u32 s15, s3
	s_cselect_b32 s3, s19, s16
	s_xor_b32 s20, s3, s18
	s_sub_i32 s3, s20, s18
	s_mul_i32 s19, s3, s9
	s_lshl_b32 s15, s3, 7
	s_sub_i32 s3, s17, s19
	s_lshl_b32 s2, s2, 6
	s_lshl_b32 s3, s3, 9
	s_and_b32 s21, s2, 0x1c0
	s_ashr_i32 s9, s8, 31
	s_movk_i32 s2, 0x70
	v_lshrrev_b32_e32 v2, 3, v0
	s_or_b32 s16, s3, s21
	s_lshl_b32 s24, s8, 1
	v_bitop3_b32 v80, v0, s2, v93 bitop3:0x48
	v_or_b32_e32 v3, s15, v2
	s_lshr_b64 s[2:3], s[8:9], 31
	v_mul_lo_u32 v8, s2, v3
	v_mad_u64_u32 v[6:7], s[22:23], s24, v3, v[4:5]
	s_ashr_i32 s3, s15, 31
	v_or_b32_e32 v3, 0x200, v0
	s_mul_i32 s3, s24, s3
	v_lshrrev_b32_e32 v3, 3, v3
	s_add_i32 s25, s16, 0xffffff80
	v_add3_u32 v7, v8, v7, s3
	v_or_b32_e32 v3, s15, v3
	v_lshl_add_u64 v[74:75], v[6:7], 0, v[80:81]
	v_mul_lo_u32 v6, s2, v3
	v_mad_u64_u32 v[82:83], s[22:23], s24, v3, v[4:5]
	v_or_b32_e32 v3, s25, v2
	v_add_u32_e32 v3, 0x80, v3
	v_ashrrev_i32_e32 v4, 31, v3
	v_add3_u32 v83, v6, v83, s3
	v_mul_lo_u32 v6, s24, v4
	v_mov_b64_e32 v[4:5], s[6:7]
	v_mul_lo_u32 v7, s2, v3
	v_mad_u64_u32 v[4:5], s[2:3], s24, v3, v[4:5]
	v_add3_u32 v5, v7, v5, v6
	v_bfe_u32 v3, v0, 5, 1
	v_lshl_add_u64 v[78:79], v[4:5], 0, v[80:81]
	v_lshl_or_b32 v4, v90, 5, v88
	v_lshlrev_b32_e32 v89, 2, v3
	v_or3_b32 v8, v4, v89, s15
	s_waitcnt lgkmcnt(0)
	s_load_dword s26, s[0:1], 0x40
	v_cmp_gt_i32_e32 vcc, s14, v8
	v_or_b32_e32 v6, 8, v8
	v_readfirstlane_b32 s2, v99
	v_cndmask_b32_e32 v4, 0, v8, vcc
	v_cmp_gt_i32_e32 vcc, s14, v6
	v_ashrrev_i32_e32 v5, 31, v4
	v_lshl_add_u64 v[4:5], v[4:5], 2, s[10:11]
	v_cndmask_b32_e32 v6, 0, v6, vcc
	v_ashrrev_i32_e32 v7, 31, v6
	v_lshl_add_u64 v[6:7], v[6:7], 2, s[10:11]
	global_load_dwordx4 v[46:49], v[4:5], off
	global_load_dwordx4 v[42:45], v[6:7], off
	v_or_b32_e32 v4, 16, v8
	v_cmp_gt_i32_e32 vcc, s14, v4
	v_or_b32_e32 v6, 24, v8
	s_mov_b32 m0, s2
	v_cndmask_b32_e32 v4, 0, v4, vcc
	v_cmp_gt_i32_e32 vcc, s14, v6
	v_ashrrev_i32_e32 v5, 31, v4
	v_lshl_add_u64 v[4:5], v[4:5], 2, s[10:11]
	v_cndmask_b32_e32 v6, 0, v6, vcc
	v_ashrrev_i32_e32 v7, 31, v6
	v_lshl_add_u64 v[6:7], v[6:7], 2, s[10:11]
	global_load_dwordx4 v[38:41], v[4:5], off
	global_load_dwordx4 v[34:37], v[6:7], off
	v_add_u32_e32 v4, 0x2000, v99
	v_lshl_add_u64 v[76:77], v[82:83], 0, v[80:81]
	v_readfirstlane_b32 s2, v4
	v_add_u32_e32 v4, 0x4000, v99
	global_load_lds_dwordx4 v[74:75], off
	s_mov_b32 m0, s2
	v_readfirstlane_b32 s2, v4
	v_add_u32_e32 v6, 0x6000, v99
	global_load_lds_dwordx4 v[76:77], off
	s_mov_b32 m0, s2
	s_mov_b64 s[2:3], 0x80
	v_readfirstlane_b32 s10, v6
	v_add_u32_e32 v6, 0x8000, v99
	global_load_lds_dwordx4 v[78:79], off
	v_lshl_add_u64 v[4:5], v[74:75], 0, s[2:3]
	s_mov_b32 m0, s10
	v_readfirstlane_b32 s10, v6
	global_load_lds_dwordx4 v[4:5], off
	v_lshl_add_u64 v[4:5], v[76:77], 0, s[2:3]
	s_mov_b32 m0, s10
	v_add_u32_e32 v6, 0xa000, v99
	global_load_lds_dwordx4 v[4:5], off
	v_lshl_add_u64 v[4:5], v[78:79], 0, s[2:3]
	v_readfirstlane_b32 s2, v6
	v_add_u32_e32 v6, 0xc000, v99
	s_mov_b32 m0, s2
	s_mov_b64 s[2:3], 0x100
	v_readfirstlane_b32 s10, v6
	v_add_u32_e32 v6, 0xe000, v99
	global_load_lds_dwordx4 v[4:5], off
	v_lshl_add_u64 v[4:5], v[74:75], 0, s[2:3]
	s_mov_b32 m0, s10
	v_readfirstlane_b32 s10, v6
	v_add_u32_e32 v6, 0x10000, v99
	global_load_lds_dwordx4 v[4:5], off
	v_lshl_add_u64 v[4:5], v[76:77], 0, s[2:3]
	s_mov_b32 m0, s10
	v_readfirstlane_b32 s10, v6
	global_load_lds_dwordx4 v[4:5], off
	v_lshl_add_u64 v[4:5], v[78:79], 0, s[2:3]
	s_mov_b32 m0, s10
	v_and_b32_e32 v91, 31, v0
	global_load_lds_dwordx4 v[4:5], off
	v_lshlrev_b32_e32 v4, 2, v90
	v_bfe_u32 v5, v0, 1, 3
	v_bitop3_b32 v3, v4, v5, v3 bitop3:0x36
	v_lshlrev_b32_e32 v4, 7, v91
	v_bfe_u32 v92, v0, 6, 1
	v_lshlrev_b32_e32 v3, 4, v3
	v_lshl_or_b32 v5, v1, 13, v4
	v_lshl_or_b32 v4, v92, 12, v4
	s_mov_b32 s10, 0
	v_add_u32_e32 v94, v5, v3
	v_add_u32_e32 v95, v4, v3
	v_add_u32_e32 v5, 0x1000, v94
	v_add_u32_e32 v3, 0x4000, v95
	s_waitcnt vmcnt(6)
	s_barrier
	v_add_u32_e32 v4, 0, v94
	ds_read_b128 v[66:69], v4
	ds_read_b128 v[62:65], v4 offset:4096
	v_add_u32_e32 v4, 0, v95
	v_xor_b32_e32 v96, 32, v94
	v_xor_b32_e32 v97, 32, v5
	v_add_u32_e32 v6, 0, v96
	ds_read_b128 v[70:73], v4 offset:16384
	ds_read_b128 v[58:61], v6
	v_add_u32_e32 v4, 0, v97
	v_xor_b32_e32 v98, 32, v3
	v_add_u32_e32 v3, 0, v98
	ds_read_b128 v[50:53], v4
	ds_read_b128 v[54:57], v3
	s_cmpk_lt_i32 s8, 0x140
	s_cbranch_scc1 .LBB6_3
	v_lshl_or_b32 v3, s20, 7, v2
	s_lshl_b32 s10, s18, 7
	v_subrev_u32_e32 v3, s10, v3
	v_mad_i64_i32 v[4:5], s[10:11], s8, v3, 0
	v_lshl_add_u64 v[84:85], v[4:5], 1, s[4:5]
	s_lshl_b32 s4, s17, 9
	s_or_b32 s4, s21, s4
	s_lshr_b32 s9, s9, 26
	v_add_u32_e32 v2, s4, v2
	s_lshl_b32 s4, s19, 9
	s_add_i32 s9, s8, s9
	v_subrev_u32_e32 v2, s4, v2
	s_ashr_i32 s9, s9, 6
	v_mad_i64_i32 v[2:3], s[4:5], s8, v2, 0
	v_mov_b32_e32 v18, 0
	s_add_i32 s9, s9, -4
	v_lshl_add_u64 v[86:87], v[2:3], 1, s[6:7]
	s_mov_b32 s10, 0
	s_mov_b64 s[4:5], 0x180
	s_mov_b64 s[6:7], 0x200
	v_mov_b32_e32 v19, v18
	v_mov_b32_e32 v20, v18
	v_mov_b32_e32 v21, v18
	v_mov_b32_e32 v22, v18
	v_mov_b32_e32 v23, v18
	v_mov_b32_e32 v24, v18
	v_mov_b32_e32 v25, v18
	v_mov_b32_e32 v26, v18
	v_mov_b32_e32 v27, v18
	v_mov_b32_e32 v28, v18
	v_mov_b32_e32 v29, v18
	v_mov_b32_e32 v30, v18
	v_mov_b32_e32 v31, v18
	v_mov_b32_e32 v32, v18
	v_mov_b32_e32 v33, v18
	v_mov_b32_e32 v2, v18
	v_mov_b32_e32 v3, v18
	v_mov_b32_e32 v4, v18
	v_mov_b32_e32 v5, v18
	v_mov_b32_e32 v6, v18
	v_mov_b32_e32 v7, v18
	v_mov_b32_e32 v8, v18
	v_mov_b32_e32 v9, v18
	v_mov_b32_e32 v10, v18
	v_mov_b32_e32 v11, v18
	v_mov_b32_e32 v12, v18
	v_mov_b32_e32 v13, v18
	v_mov_b32_e32 v14, v18
	v_mov_b32_e32 v15, v18
	v_mov_b32_e32 v16, v18
	v_mov_b32_e32 v17, v18

.LBB6_8:
	s_or_b64 exec, exec, s[6:7]
	s_mov_b32 s0, s26
	v_lshlrev_b32_e32 v0, 5, v92
	v_lshlrev_b32_e32 v51, 12, v80
	v_or3_b32 v52, v91, v0, s16
	v_mov_b64_e32 v[0:1], s[12:13]
	v_or3_b32 v68, v88, v89, s15
	s_waitcnt lgkmcnt(0)
	v_mad_i64_i32 v[0:1], s[0:1], v52, s0, v[0:1]
	v_add_u32_e32 v69, v50, v51
	s_barrier
	s_and_saveexec_b64 s[4:5], s[2:3]
	s_cbranch_execnz .LBB6_11
	s_or_b64 exec, exec, s[4:5]
	s_and_saveexec_b64 s[0:1], vcc
	s_cbranch_execnz .LBB6_20

amdhsa.kernels:
  - .agpr_count:     0
    .args:
      - .actual_access:  read_only
        .address_space:  global
        .offset:         0
        .size:           8
        .value_kind:     global_buffer
      - .actual_access:  write_only
        .address_space:  global
        .offset:         8
        .size:           8
        .value_kind:     global_buffer
      - .actual_access:  read_only
        .address_space:  global
        .offset:         16
        .size:           8
        .value_kind:     global_buffer
      - .actual_access:  read_only
        .address_space:  global
        .offset:         24
        .size:           8
        .value_kind:     global_buffer
      - .actual_access:  read_only
        .address_space:  global
        .offset:         32
        .size:           8
        .value_kind:     global_buffer
      - .actual_access:  write_only
        .address_space:  global
        .offset:         40
        .size:           8
        .value_kind:     global_buffer
      - .actual_access:  write_only
        .address_space:  global
        .offset:         48
        .size:           8
        .value_kind:     global_buffer
      - .actual_access:  write_only
        .address_space:  global
        .offset:         56
        .size:           8
        .value_kind:     global_buffer
      - .actual_access:  write_only
        .address_space:  global
        .offset:         64
        .size:           8
        .value_kind:     global_buffer
      - .actual_access:  write_only
        .address_space:  global
        .offset:         72
        .size:           8
        .value_kind:     global_buffer
      - .actual_access:  write_only
        .address_space:  global
        .offset:         80
        .size:           8
        .value_kind:     global_buffer
    .group_segment_fixed_size: 16640
    .kernarg_segment_align: 8
    .kernarg_segment_size: 88
    .language:       OpenCL C
    .language_version:
      - 2
      - 0
    .max_flat_workgroup_size: 256
    .name:           _Z8prep_allPKfPcS0_S0_S0_S1_S1_S1_PyPiS3_
    .private_segment_fixed_size: 0
    .sgpr_count:     30
    .sgpr_spill_count: 0
    .symbol:         _Z8prep_allPKfPcS0_S0_S0_S1_S1_S1_PyPiS3_.kd
    .uniform_work_group_size: 1
    .uses_dynamic_stack: false
    .vgpr_count:     48
    .vgpr_spill_count: 0
    .wavefront_size: 64
  - .agpr_count:     0
    .args:
      - .actual_access:  read_only
        .address_space:  global
        .offset:         0
        .size:           8
        .value_kind:     global_buffer
      - .actual_access:  write_only
        .address_space:  global
        .offset:         8
        .size:           8
        .value_kind:     global_buffer
      - .actual_access:  write_only
        .address_space:  global
        .offset:         16
        .size:           8
        .value_kind:     global_buffer
      - .address_space:  global
        .offset:         24
        .size:           8
        .value_kind:     global_buffer
    .group_segment_fixed_size: 0
    .kernarg_segment_align: 8
    .kernarg_segment_size: 32
    .language:       OpenCL C
    .language_version:
      - 2
      - 0
    .max_flat_workgroup_size: 256
    .name:           _Z13select_kernelPKfPyPiS2_
    .private_segment_fixed_size: 0
    .sgpr_count:     21
    .sgpr_spill_count: 0
    .symbol:         _Z13select_kernelPKfPyPiS2_.kd
    .uniform_work_group_size: 1
    .uses_dynamic_stack: false
    .vgpr_count:     16
    .vgpr_spill_count: 0
    .wavefront_size: 64
  - .agpr_count:     0
    .args:
      - .actual_access:  read_only
        .address_space:  global
        .offset:         0
        .size:           8
        .value_kind:     global_buffer
      - .actual_access:  write_only
        .address_space:  global
        .offset:         8
        .size:           8
        .value_kind:     global_buffer
      - .actual_access:  write_only
        .address_space:  global
        .offset:         16
        .size:           8
        .value_kind:     global_buffer
      - .actual_access:  write_only
        .address_space:  global
        .offset:         24
        .size:           8
        .value_kind:     global_buffer
    .group_segment_fixed_size: 4128
    .kernarg_segment_align: 8
    .kernarg_segment_size: 32
    .language:       OpenCL C
    .language_version:
      - 2
      - 0
    .max_flat_workgroup_size: 1024
    .name:           _Z12route_kernelPKyPiP15HIP_vector_typeIiLj4EES1_
    .private_segment_fixed_size: 0
    .sgpr_count:     19
    .sgpr_spill_count: 0
    .symbol:         _Z12route_kernelPKyPiP15HIP_vector_typeIiLj4EES1_.kd
    .uniform_work_group_size: 1
    .uses_dynamic_stack: false
    .vgpr_count:     23
    .vgpr_spill_count: 0
    .wavefront_size: 64
  - .agpr_count:     66
    .args:
      - .actual_access:  read_only
        .address_space:  global
        .offset:         0
        .size:           8
        .value_kind:     global_buffer
      - .actual_access:  read_only
        .address_space:  global
        .offset:         8
        .size:           8
        .value_kind:     global_buffer
      - .actual_access:  read_only
        .address_space:  global
        .offset:         16
        .size:           8
        .value_kind:     global_buffer
      - .actual_access:  read_only
        .address_space:  global
        .offset:         24
        .size:           8
        .value_kind:     global_buffer
      - .actual_access:  read_only
        .address_space:  global
        .offset:         32
        .size:           8
        .value_kind:     global_buffer
      - .actual_access:  write_only
        .address_space:  global
        .offset:         40
        .size:           8
        .value_kind:     global_buffer
    .group_segment_fixed_size: 51200
    .kernarg_segment_align: 8
    .kernarg_segment_size: 48
    .language:       OpenCL C
    .language_version:
      - 2
      - 0
    .max_flat_workgroup_size: 256
    .name:           _Z13expert_kernelPKcPKfPKiPK15HIP_vector_typeIiLj4EES4_Pf
    .private_segment_fixed_size: 0
    .sgpr_count:     20
    .sgpr_spill_count: 0
    .symbol:         _Z13expert_kernelPKcPKfPKiPK15HIP_vector_typeIiLj4EES4_Pf.kd
    .uniform_work_group_size: 1
    .uses_dynamic_stack: false
    .vgpr_count:     158
    .vgpr_spill_count: 0
    .wavefront_size: 64
  - .agpr_count:     0
    .args:
      - .actual_access:  read_only
        .address_space:  global
        .offset:         0
        .size:           8
        .value_kind:     global_buffer
      - .actual_access:  read_only
        .address_space:  global
        .offset:         8
        .size:           8
        .value_kind:     global_buffer
      - .actual_access:  read_only
        .address_space:  global
        .offset:         16
        .size:           8
        .value_kind:     global_buffer
      - .actual_access:  read_only
        .address_space:  global
        .offset:         24
        .size:           8
        .value_kind:     global_buffer
      - .actual_access:  read_only
        .address_space:  global
        .offset:         32
        .size:           8
        .value_kind:     global_buffer
      - .actual_access:  read_only
        .address_space:  global
        .offset:         40
        .size:           8
        .value_kind:     global_buffer
      - .actual_access:  read_only
        .address_space:  global
        .offset:         48
        .size:           8
        .value_kind:     global_buffer
      - .actual_access:  read_only
        .address_space:  global
        .offset:         56
        .size:           8
        .value_kind:     global_buffer
      - .actual_access:  read_only
        .address_space:  global
        .offset:         64
        .size:           8
        .value_kind:     global_buffer
      - .actual_access:  write_only
        .address_space:  global
        .offset:         72
        .size:           8
        .value_kind:     global_buffer
    .group_segment_fixed_size: 14000
    .kernarg_segment_align: 8
    .kernarg_segment_size: 80
    .language:       OpenCL C
    .language_version:
      - 2
      - 0
    .max_flat_workgroup_size: 256
    .name:           _Z12final_kernelPKfPKiPK15HIP_vector_typeIiLj4EES2_S2_S0_S0_S0_S0_Pf
    .private_segment_fixed_size: 0
    .sgpr_count:     50
    .sgpr_spill_count: 0
    .symbol:         _Z12final_kernelPKfPKiPK15HIP_vector_typeIiLj4EES2_S2_S0_S0_S0_S0_Pf.kd
    .uniform_work_group_size: 1
    .uses_dynamic_stack: false
    .vgpr_count:     140
    .vgpr_spill_count: 0
    .wavefront_size: 64
  - .agpr_count:     0
    .args:
      - .address_space:  global
        .offset:         0
        .size:           8
        .value_kind:     global_buffer
      - .address_space:  global
        .offset:         8
        .size:           8
        .value_kind:     global_buffer
      - .offset:         16
        .size:           4
        .value_kind:     by_value
      - .offset:         20
        .size:           4
        .value_kind:     by_value
      - .actual_access:  read_only
        .address_space:  global
        .offset:         24
        .size:           8
        .value_kind:     global_buffer
      - .offset:         32
        .size:           4
        .value_kind:     by_value
      - .actual_access:  read_only
        .address_space:  global
        .offset:         40
        .size:           8
        .value_kind:     global_buffer
      - .actual_access:  read_only
        .address_space:  global
        .offset:         48
        .size:           8
        .value_kind:     global_buffer
      - .actual_access:  write_only
        .address_space:  global
        .offset:         56
        .size:           8
        .value_kind:     global_buffer
      - .offset:         64
        .size:           4
        .value_kind:     by_value
      - .actual_access:  read_only
        .address_space:  global
        .offset:         72
        .size:           8
        .value_kind:     global_buffer
    .group_segment_fixed_size: 0
    .kernarg_segment_align: 8
    .kernarg_segment_size: 80
    .language:       OpenCL C
    .language_version:
      - 2
      - 0
    .max_flat_workgroup_size: 512
    .name:           _Z7gemm_x3ILi2ELi2ELi2ELi0EEvPKcS1_iiPKfiS3_PKiPciPy
    .private_segment_fixed_size: 0
    .sgpr_count:     38
    .sgpr_spill_count: 0
    .symbol:         _Z7gemm_x3ILi2ELi2ELi2ELi0EEvPKcS1_iiPKfiS3_PKiPciPy.kd
    .uniform_work_group_size: 1
    .uses_dynamic_stack: false
    .vgpr_count:     208
    .vgpr_spill_count: 0
    .wavefront_size: 64
  - .agpr_count:     0
    .args:
      - .address_space:  global
        .offset:         0
        .size:           8
        .value_kind:     global_buffer
      - .address_space:  global
        .offset:         8
        .size:           8
        .value_kind:     global_buffer
      - .offset:         16
        .size:           4
        .value_kind:     by_value
      - .offset:         20
        .size:           4
        .value_kind:     by_value
      - .actual_access:  read_only
        .address_space:  global
        .offset:         24
        .size:           8
        .value_kind:     global_buffer
      - .offset:         32
        .size:           4
        .value_kind:     by_value
      - .actual_access:  read_only
        .address_space:  global
        .offset:         40
        .size:           8
        .value_kind:     global_buffer
      - .actual_access:  read_only
        .address_space:  global
        .offset:         48
        .size:           8
        .value_kind:     global_buffer
      - .actual_access:  write_only
        .address_space:  global
        .offset:         56
        .size:           8
        .value_kind:     global_buffer
      - .offset:         64
        .size:           4
        .value_kind:     by_value
      - .actual_access:  read_only
        .address_space:  global
        .offset:         72
        .size:           8
        .value_kind:     global_buffer
    .group_segment_fixed_size: 0
    .kernarg_segment_align: 8
    .kernarg_segment_size: 80
    .language:       OpenCL C
    .language_version:
      - 2
      - 0
    .max_flat_workgroup_size: 512
    .name:           _Z7gemm_x3ILi2ELi2ELi1ELi1EEvPKcS1_iiPKfiS3_PKiPciPy
    .private_segment_fixed_size: 0
    .sgpr_count:     33
    .sgpr_spill_count: 0
    .symbol:         _Z7gemm_x3ILi2ELi2ELi1ELi1EEvPKcS1_iiPKfiS3_PKiPciPy.kd
    .uniform_work_group_size: 1
    .uses_dynamic_stack: false
    .vgpr_count:     114
    .vgpr_spill_count: 0
    .wavefront_size: 64
  - .agpr_count:     32
    .args:
      - .address_space:  global
        .offset:         0
        .size:           8
        .value_kind:     global_buffer
      - .address_space:  global
        .offset:         8
        .size:           8
        .value_kind:     global_buffer
      - .offset:         16
        .size:           4
        .value_kind:     by_value
      - .offset:         20
        .size:           4
        .value_kind:     by_value
      - .actual_access:  read_only
        .address_space:  global
        .offset:         24
        .size:           8
        .value_kind:     global_buffer
      - .offset:         32
        .size:           4
        .value_kind:     by_value
      - .actual_access:  read_only
        .address_space:  global
        .offset:         40
        .size:           8
        .value_kind:     global_buffer
      - .actual_access:  read_only
        .address_space:  global
        .offset:         48
        .size:           8
        .value_kind:     global_buffer
      - .actual_access:  write_only
        .address_space:  global
        .offset:         56
        .size:           8
        .value_kind:     global_buffer
      - .offset:         64
        .size:           4
        .value_kind:     by_value
      - .address_space:  global
        .offset:         72
        .size:           8
        .value_kind:     global_buffer
    .group_segment_fixed_size: 0
    .kernarg_segment_align: 8
    .kernarg_segment_size: 80
    .language:       OpenCL C
    .language_version:
      - 2
      - 0
    .max_flat_workgroup_size: 256
    .name:           _Z7gemm_x3ILi1ELi2ELi1ELi2EEvPKcS1_iiPKfiS3_PKiPciPy
    .private_segment_fixed_size: 0
    .sgpr_count:     29
    .sgpr_spill_count: 0
    .symbol:         _Z7gemm_x3ILi1ELi2ELi1ELi2EEvPKcS1_iiPKfiS3_PKiPciPy.kd
    .uniform_work_group_size: 1
    .uses_dynamic_stack: false
    .vgpr_count:     136
    .vgpr_spill_count: 0
    .wavefront_size: 64
  - .agpr_count:     0
    .args:
      - .actual_access:  read_only
        .address_space:  global
        .offset:         0
        .size:           8
        .value_kind:     global_buffer
      - .offset:         8
        .size:           4
        .value_kind:     by_value
      - .offset:         12
        .size:           4
        .value_kind:     by_value
      - .actual_access:  read_only
        .address_space:  global
        .offset:         16
        .size:           8
        .value_kind:     global_buffer
      - .offset:         24
        .size:           4
        .value_kind:     by_value
      - .offset:         28
        .size:           4
        .value_kind:     by_value
      - .actual_access:  read_only
        .address_space:  global
        .offset:         32
        .size:           8
        .value_kind:     global_buffer
      - .actual_access:  read_only
        .address_space:  global
        .offset:         40
        .size:           8
        .value_kind:     global_buffer
      - .actual_access:  read_only
        .address_space:  global
        .offset:         48
        .size:           8
        .value_kind:     global_buffer
      - .actual_access:  read_only
        .address_space:  global
        .offset:         56
        .size:           8
        .value_kind:     global_buffer
      - .actual_access:  write_only
        .address_space:  global
        .offset:         64
        .size:           8
        .value_kind:     global_buffer
      - .offset:         72
        .size:           4
        .value_kind:     by_value
      - .actual_access:  read_only
        .address_space:  global
        .offset:         80
        .size:           8
        .value_kind:     global_buffer
      - .offset:         88
        .size:           4
        .value_kind:     hidden_block_count_x
      - .offset:         92
        .size:           4
        .value_kind:     hidden_block_count_y
      - .offset:         96
        .size:           4
        .value_kind:     hidden_block_count_z
      - .offset:         100
        .size:           2
        .value_kind:     hidden_group_size_x
      - .offset:         102
        .size:           2
        .value_kind:     hidden_group_size_y
      - .offset:         104
        .size:           2
        .value_kind:     hidden_group_size_z
      - .offset:         106
        .size:           2
        .value_kind:     hidden_remainder_x
      - .offset:         108
        .size:           2
        .value_kind:     hidden_remainder_y
      - .offset:         110
        .size:           2
        .value_kind:     hidden_remainder_z
      - .offset:         128
        .size:           8
        .value_kind:     hidden_global_offset_x
      - .offset:         136
        .size:           8
        .value_kind:     hidden_global_offset_y
      - .offset:         144
        .size:           8
        .value_kind:     hidden_global_offset_z
      - .offset:         152
        .size:           2
        .value_kind:     hidden_grid_dims
    .group_segment_fixed_size: 16384
    .kernarg_segment_align: 8
    .kernarg_segment_size: 344
    .language:       OpenCL C
    .language_version:
      - 2
      - 0
    .max_flat_workgroup_size: 1024
    .name:           _Z13refine_kernelILi1ELi16ELi128ELb1ELi4EEvPKfiiS1_iiS1_PKiS3_S3_PfiPy
    .private_segment_fixed_size: 0
    .sgpr_count:     35
    .sgpr_spill_count: 0
    .symbol:         _Z13refine_kernelILi1ELi16ELi128ELb1ELi4EEvPKfiiS1_iiS1_PKiS3_S3_PfiPy.kd
    .uniform_work_group_size: 1
    .uses_dynamic_stack: false
    .vgpr_count:     64
    .vgpr_spill_count: 0
    .wavefront_size: 64
  - .agpr_count:     0
    .args:
      - .actual_access:  read_only
        .address_space:  global
        .offset:         0
        .size:           8
        .value_kind:     global_buffer
      - .offset:         8
        .size:           4
        .value_kind:     by_value
      - .offset:         12
        .size:           4
        .value_kind:     by_value
      - .actual_access:  read_only
        .address_space:  global
        .offset:         16
        .size:           8
        .value_kind:     global_buffer
      - .offset:         24
        .size:           4
        .value_kind:     by_value
      - .offset:         28
        .size:           4
        .value_kind:     by_value
      - .actual_access:  read_only
        .address_space:  global
        .offset:         32
        .size:           8
        .value_kind:     global_buffer
      - .actual_access:  read_only
        .address_space:  global
        .offset:         40
        .size:           8
        .value_kind:     global_buffer
      - .actual_access:  read_only
        .address_space:  global
        .offset:         48
        .size:           8
        .value_kind:     global_buffer
      - .actual_access:  read_only
        .address_space:  global
        .offset:         56
        .size:           8
        .value_kind:     global_buffer
      - .actual_access:  write_only
        .address_space:  global
        .offset:         64
        .size:           8
        .value_kind:     global_buffer
      - .offset:         72
        .size:           4
        .value_kind:     by_value
      - .actual_access:  read_only
        .address_space:  global
        .offset:         80
        .size:           8
        .value_kind:     global_buffer
      - .offset:         88
        .size:           4
        .value_kind:     hidden_block_count_x
      - .offset:         92
        .size:           4
        .value_kind:     hidden_block_count_y
      - .offset:         96
        .size:           4
        .value_kind:     hidden_block_count_z
      - .offset:         100
        .size:           2
        .value_kind:     hidden_group_size_x
      - .offset:         102
        .size:           2
        .value_kind:     hidden_group_size_y
      - .offset:         104
        .size:           2
        .value_kind:     hidden_group_size_z
      - .offset:         106
        .size:           2
        .value_kind:     hidden_remainder_x
      - .offset:         108
        .size:           2
        .value_kind:     hidden_remainder_y
      - .offset:         110
        .size:           2
        .value_kind:     hidden_remainder_z
      - .offset:         128
        .size:           8
        .value_kind:     hidden_global_offset_x
      - .offset:         136
        .size:           8
        .value_kind:     hidden_global_offset_y
      - .offset:         144
        .size:           8
        .value_kind:     hidden_global_offset_z
      - .offset:         152
        .size:           2
        .value_kind:     hidden_grid_dims
    .group_segment_fixed_size: 16384
    .kernarg_segment_align: 8
    .kernarg_segment_size: 344
    .language:       OpenCL C
    .language_version:
      - 2
      - 0
    .max_flat_workgroup_size: 1024
    .name:           _Z13refine_kernelILi2ELi16ELi64ELb0ELi4EEvPKfiiS1_iiS1_PKiS3_S3_PfiPy
    .private_segment_fixed_size: 0
    .sgpr_count:     35
    .sgpr_spill_count: 0
    .symbol:         _Z13refine_kernelILi2ELi16ELi64ELb0ELi4EEvPKfiiS1_iiS1_PKiS3_S3_PfiPy.kd
    .uniform_work_group_size: 1
    .uses_dynamic_stack: false
    .vgpr_count:     85
    .vgpr_spill_count: 0
    .wavefront_size: 64
  - .agpr_count:     0
    .args:
      - .actual_access:  read_only
        .address_space:  global
        .offset:         0
        .size:           8
        .value_kind:     global_buffer
      - .offset:         8
        .size:           4
        .value_kind:     by_value
      - .offset:         12
        .size:           4
        .value_kind:     by_value
      - .actual_access:  read_only
        .address_space:  global
        .offset:         16
        .size:           8
        .value_kind:     global_buffer
      - .offset:         24
        .size:           4
        .value_kind:     by_value
      - .offset:         28
        .size:           4
        .value_kind:     by_value
      - .actual_access:  read_only
        .address_space:  global
        .offset:         32
        .size:           8
        .value_kind:     global_buffer
      - .actual_access:  read_only
        .address_space:  global
        .offset:         40
        .size:           8
        .value_kind:     global_buffer
      - .actual_access:  read_only
        .address_space:  global
        .offset:         48
        .size:           8
        .value_kind:     global_buffer
      - .actual_access:  read_only
        .address_space:  global
        .offset:         56
        .size:           8
        .value_kind:     global_buffer
      - .actual_access:  read_only
        .address_space:  global
        .offset:         64
        .size:           8
        .value_kind:     global_buffer
      - .offset:         72
        .size:           4
        .value_kind:     by_value
      - .address_space:  global
        .offset:         80
        .size:           8
        .value_kind:     global_buffer
      - .offset:         88
        .size:           4
        .value_kind:     hidden_block_count_x
      - .offset:         92
        .size:           4
        .value_kind:     hidden_block_count_y
      - .offset:         96
        .size:           4
        .value_kind:     hidden_block_count_z
      - .offset:         100
        .size:           2
        .value_kind:     hidden_group_size_x
      - .offset:         102
        .size:           2
        .value_kind:     hidden_group_size_y
      - .offset:         104
        .size:           2
        .value_kind:     hidden_group_size_z
      - .offset:         106
        .size:           2
        .value_kind:     hidden_remainder_x
      - .offset:         108
        .size:           2
        .value_kind:     hidden_remainder_y
      - .offset:         110
        .size:           2
        .value_kind:     hidden_remainder_z
      - .offset:         128
        .size:           8
        .value_kind:     hidden_global_offset_x
      - .offset:         136
        .size:           8
        .value_kind:     hidden_global_offset_y
      - .offset:         144
        .size:           8
        .value_kind:     hidden_global_offset_z
      - .offset:         152
        .size:           2
        .value_kind:     hidden_grid_dims
    .group_segment_fixed_size: 8192
    .kernarg_segment_align: 8
    .kernarg_segment_size: 344
    .language:       OpenCL C
    .language_version:
      - 2
      - 0
    .max_flat_workgroup_size: 512
    .name:           _Z13refine_kernelILi3ELi8ELi64ELb0ELi4EEvPKfiiS1_iiS1_PKiS3_S3_PfiPy
    .private_segment_fixed_size: 0
    .sgpr_count:     38
    .sgpr_spill_count: 0
    .symbol:         _Z13refine_kernelILi3ELi8ELi64ELb0ELi4EEvPKfiiS1_iiS1_PKiS3_S3_PfiPy.kd
    .uniform_work_group_size: 1
    .uses_dynamic_stack: false
    .vgpr_count:     88
    .vgpr_spill_count: 0
    .wavefront_size: 64
